# retention prep: the three first-iteration-only vmcnt waits in front of the round-1 register copies removed (preheader drains instead); v29 otherwise
# speedup vs baseline: 1.0037x; 1.0037x over previous
.LBB0_890:
	s_or_b64 exec, exec, s[20:21]
	v_readfirstlane_b32 s8, v0
	s_cmpk_gt_i32 s8, 0xff
	s_cbranch_scc1 .LBB0_922
	s_mul_i32 s20, s72, 0x1e00000
	v_lshlrev_b32_e32 v0, 1, v190
	s_mul_hi_i32 s9, s72, 0x1e00000
	s_add_u32 s20, s74, s20
	v_lshl_or_b32 v128, s1, 7, v0
	v_cvt_f32_ubyte0_e32 v0, s1
	s_addc_u32 s21, s75, s9
	v_sub_f32_e32 v0, 0xc0a00000, v0
	s_mov_b32 s9, 0xc2fc0000
	v_cmp_gt_f32_e32 vcc, s9, v0
	v_lshl_add_u64 v[84:85], s[20:21], 0, v[128:129]
	s_and_b64 s[20:21], vcc, exec
	v_cndmask_b32_e32 v1, 0, v213, vcc
	v_add_f32_e32 v0, v0, v1
	v_exp_f32_e32 v0, v0
	s_cselect_b32 s9, 0xffffffc0, 0
	v_mov_b32_e32 v1, 0x42000000
	v_ldexp_f32 v0, v0, s9
	v_sub_f32_e32 v0, 1.0, v0
	v_cmp_gt_f32_e32 vcc, s19, v0
	s_and_b64 s[20:21], vcc, exec
	s_cselect_b32 s9, 32, 0
	v_ldexp_f32 v0, v0, s9
	v_log_f32_e32 v0, v0
	v_cndmask_b32_e32 v1, 0, v1, vcc
	s_lshl_b32 s9, s8, 4
	v_add_u32_e32 v8, s9, v192
	v_sub_f32_e32 v52, v0, v1
	v_add_u32_e32 v0, s9, v188
	v_mul_f32_e32 v53, v52, v197
	v_ashrrev_i32_e32 v1, 31, v0
	v_mad_i64_i32 v[2:3], s[20:21], v0, s11, v[84:85]
	global_load_dwordx4 v[40:43], v[2:3], off offset:3584
	v_add_co_u32_e32 v2, vcc, s7, v2
	v_lshlrev_b64 v[0:1], 8, v[0:1]
	s_nop 0
	v_addc_co_u32_e32 v3, vcc, 0, v3, vcc
	v_lshl_add_u64 v[0:1], v[174:175], 0, v[0:1]
	global_load_dwordx4 v[36:39], v[2:3], off offset:512
	global_load_dwordx4 v[28:31], v[2:3], off offset:1536
	global_load_dwordx4 v[32:35], v[0:1], off offset:48
	global_load_dwordx4 v[44:47], v[0:1], off offset:32
	global_load_dwordx4 v[48:51], v[0:1], off offset:16
	global_load_dwordx4 v[80:83], v[0:1], off
	v_exp_f32_e32 v86, v53
	v_ashrrev_i32_e32 v9, 31, v8
	v_mad_i64_i32 v[0:1], s[20:21], v8, s11, v[84:85]
	global_load_dwordx4 v[12:15], v[0:1], off offset:3584
	v_add_co_u32_e32 v0, vcc, s7, v0
	v_lshlrev_b64 v[8:9], 8, v[8:9]
	s_nop 0
	v_addc_co_u32_e32 v1, vcc, 0, v1, vcc
	v_lshl_add_u64 v[24:25], v[174:175], 0, v[8:9]
	global_load_dwordx4 v[4:7], v[0:1], off offset:512
	s_nop 0
	global_load_dwordx4 v[0:3], v[0:1], off offset:1536
	s_nop 0
	global_load_dwordx4 v[8:11], v[24:25], off offset:48
	global_load_dwordx4 v[16:19], v[24:25], off offset:32
	global_load_dwordx4 v[20:23], v[24:25], off offset:16
	s_nop 0
	global_load_dwordx4 v[24:27], v[24:25], off
	v_mul_f32_e64 v53, v52, -v197
	v_exp_f32_e32 v53, v53
	v_mov_b32_e32 v87, v86
	v_mul_f32_e32 v88, 0x3e000000, v53
	v_mul_f32_e32 v53, v52, v201
	v_mul_f32_e64 v52, v52, -v201
	v_exp_f32_e32 v52, v52
	v_exp_f32_e32 v90, v53
	v_mov_b32_e32 v89, v88
	v_mul_f32_e32 v92, 0x3e000000, v52
	v_mov_b32_e32 v93, v92
	v_mov_b32_e32 v91, v90
	s_waitcnt vmcnt(0)
	s_branch .LBB0_893

.LBB0_918:
	v_lshlrev_b32_e32 v96, 16, v40
	v_and_b32_e32 v97, 0xffff0000, v40
	v_mov_b32_e32 v101, v82
	v_mov_b32_dpp v40, v96 row_half_mirror row_mask:0xf bank_mask:0xf bound_ctrl:1
	v_mov_b32_e32 v82, v81
	v_mov_b32_e32 v100, v80
	v_mov_b32_dpp v98, v40 quad_perm:[3,2,1,0] row_mask:0xf bank_mask:0xf bound_ctrl:1
	v_mov_b32_dpp v40, v97 row_half_mirror row_mask:0xf bank_mask:0xf bound_ctrl:1
	s_mul_hi_i32 s30, s8, 0x66666667
	s_lshr_b32 s31, s30, 31
	v_mov_b32_dpp v99, v40 quad_perm:[3,2,1,0] row_mask:0xf bank_mask:0xf bound_ctrl:1
	v_pk_mul_f32 v[80:81], v[82:83], v[98:99]
	v_lshlrev_b32_e32 v40, 16, v41
	v_cndmask_b32_e64 v81, v81, -v81, s[38:39]
	v_cndmask_b32_e64 v80, v80, -v80, s[38:39]
	v_pk_fma_f32 v[80:81], v[100:101], v[96:97], v[80:81]
	v_lshlrev_b32_e32 v96, 16, v36
	v_and_b32_e32 v97, 0xffff0000, v36
	v_and_b32_e32 v41, 0xffff0000, v41
	v_mov_b32_dpp v36, v96 row_half_mirror row_mask:0xf bank_mask:0xf bound_ctrl:1
	s_ashr_i32 s30, s30, 2
	s_add_i32 s30, s30, s31
	v_mov_b32_dpp v98, v36 quad_perm:[3,2,1,0] row_mask:0xf bank_mask:0xf bound_ctrl:1
	v_mov_b32_dpp v36, v97 row_half_mirror row_mask:0xf bank_mask:0xf bound_ctrl:1
	s_mul_i32 s30, s30, 10
	s_sub_i32 s30, s8, s30
	v_mov_b32_dpp v99, v36 quad_perm:[3,2,1,0] row_mask:0xf bank_mask:0xf bound_ctrl:1
	v_pk_mul_f32 v[82:83], v[82:83], v[98:99]
	v_mov_b32_dpp v36, v40 row_half_mirror row_mask:0xf bank_mask:0xf bound_ctrl:1
	v_cndmask_b32_e64 v83, v83, -v83, s[38:39]
	v_cndmask_b32_e64 v82, v82, -v82, s[38:39]
	v_pk_fma_f32 v[82:83], v[100:101], v[96:97], v[82:83]
	v_mov_b32_dpp v96, v36 quad_perm:[3,2,1,0] row_mask:0xf bank_mask:0xf bound_ctrl:1
	v_mov_b32_dpp v36, v41 row_half_mirror row_mask:0xf bank_mask:0xf bound_ctrl:1
	v_mov_b32_e32 v99, v50
	v_mov_b32_e32 v50, v49
	v_mov_b32_dpp v97, v36 quad_perm:[3,2,1,0] row_mask:0xf bank_mask:0xf bound_ctrl:1
	v_mov_b32_e32 v98, v48
	v_pk_mul_f32 v[48:49], v[50:51], v[96:97]
	v_lshlrev_b32_e32 v36, 16, v37
	v_cndmask_b32_e64 v49, v49, -v49, s[38:39]
	v_cndmask_b32_e64 v48, v48, -v48, s[38:39]
	v_and_b32_e32 v37, 0xffff0000, v37
	v_pk_fma_f32 v[40:41], v[98:99], v[40:41], v[48:49]
	v_mov_b32_dpp v48, v36 row_half_mirror row_mask:0xf bank_mask:0xf bound_ctrl:1
	v_mov_b32_dpp v49, v37 row_half_mirror row_mask:0xf bank_mask:0xf bound_ctrl:1
	v_mov_b32_e32 v97, v46
	v_mov_b32_dpp v48, v48 quad_perm:[3,2,1,0] row_mask:0xf bank_mask:0xf bound_ctrl:1
	v_mov_b32_dpp v49, v49 quad_perm:[3,2,1,0] row_mask:0xf bank_mask:0xf bound_ctrl:1
	v_pk_mul_f32 v[48:49], v[50:51], v[48:49]
	v_mov_b32_e32 v46, v45
	v_cndmask_b32_e64 v49, v49, -v49, s[38:39]
	v_cndmask_b32_e64 v48, v48, -v48, s[38:39]
	v_pk_fma_f32 v[36:37], v[98:99], v[36:37], v[48:49]
	v_lshlrev_b32_e32 v48, 16, v42
	v_and_b32_e32 v49, 0xffff0000, v42
	v_mov_b32_e32 v96, v44
	v_mov_b32_dpp v42, v48 row_half_mirror row_mask:0xf bank_mask:0xf bound_ctrl:1
	s_mul_i32 s31, s30, 0x3200
	s_add_i32 s31, s31, 0
	v_mov_b32_dpp v50, v42 quad_perm:[3,2,1,0] row_mask:0xf bank_mask:0xf bound_ctrl:1
	v_mov_b32_dpp v42, v49 row_half_mirror row_mask:0xf bank_mask:0xf bound_ctrl:1
	v_add_u32_e32 v95, s31, v193
	v_pk_mul_f32 v[80:81], v[86:87], v[80:81]
	v_mov_b32_dpp v51, v42 quad_perm:[3,2,1,0] row_mask:0xf bank_mask:0xf bound_ctrl:1
	v_pk_mul_f32 v[44:45], v[46:47], v[50:51]
	v_lshlrev_b32_e32 v42, 16, v43
	v_cndmask_b32_e64 v45, v45, -v45, s[38:39]
	v_cndmask_b32_e64 v44, v44, -v44, s[38:39]
	v_pk_fma_f32 v[44:45], v[96:97], v[48:49], v[44:45]
	v_lshlrev_b32_e32 v48, 16, v38
	v_and_b32_e32 v49, 0xffff0000, v38
	v_and_b32_e32 v43, 0xffff0000, v43
	v_mov_b32_dpp v38, v48 row_half_mirror row_mask:0xf bank_mask:0xf bound_ctrl:1
	v_pk_mul_f32 v[82:83], v[88:89], v[82:83]
	v_pk_mul_f32 v[40:41], v[86:87], v[40:41]
	v_mov_b32_dpp v50, v38 quad_perm:[3,2,1,0] row_mask:0xf bank_mask:0xf bound_ctrl:1
	v_mov_b32_dpp v38, v49 row_half_mirror row_mask:0xf bank_mask:0xf bound_ctrl:1
	v_pk_mul_f32 v[36:37], v[88:89], v[36:37]
	v_pk_mul_f32 v[44:45], v[86:87], v[44:45]
	v_mov_b32_dpp v51, v38 quad_perm:[3,2,1,0] row_mask:0xf bank_mask:0xf bound_ctrl:1
	v_pk_mul_f32 v[46:47], v[46:47], v[50:51]
	v_mov_b32_dpp v38, v42 row_half_mirror row_mask:0xf bank_mask:0xf bound_ctrl:1
	v_cndmask_b32_e64 v47, v47, -v47, s[38:39]
	v_cndmask_b32_e64 v46, v46, -v46, s[38:39]
	v_pk_fma_f32 v[46:47], v[96:97], v[48:49], v[46:47]
	v_mov_b32_dpp v48, v38 quad_perm:[3,2,1,0] row_mask:0xf bank_mask:0xf bound_ctrl:1
	v_mov_b32_dpp v38, v43 row_half_mirror row_mask:0xf bank_mask:0xf bound_ctrl:1
	v_mov_b32_e32 v51, v34
	v_mov_b32_e32 v34, v33
	v_mov_b32_dpp v49, v38 quad_perm:[3,2,1,0] row_mask:0xf bank_mask:0xf bound_ctrl:1
	v_mov_b32_e32 v50, v32
	v_pk_mul_f32 v[32:33], v[34:35], v[48:49]
	v_pk_mul_f32 v[46:47], v[88:89], v[46:47]
	v_cndmask_b32_e64 v33, v33, -v33, s[38:39]
	v_cndmask_b32_e64 v32, v32, -v32, s[38:39]
	v_pk_fma_f32 v[32:33], v[50:51], v[42:43], v[32:33]
	v_add_u32_e32 v95, v95, v200
	v_pk_mul_f32 v[42:43], v[86:87], v[32:33]
	v_lshlrev_b32_e32 v32, 16, v39
	v_and_b32_e32 v33, 0xffff0000, v39
	ds_write_b128 v95, v[28:31] offset:10496
	v_mov_b32_dpp v38, v32 row_half_mirror row_mask:0xf bank_mask:0xf bound_ctrl:1
	v_mov_b32_dpp v39, v33 row_half_mirror row_mask:0xf bank_mask:0xf bound_ctrl:1
	v_cvt_pk_bf16_f32 v28, v80, v81
	v_mov_b32_dpp v38, v38 quad_perm:[3,2,1,0] row_mask:0xf bank_mask:0xf bound_ctrl:1
	v_mov_b32_dpp v39, v39 quad_perm:[3,2,1,0] row_mask:0xf bank_mask:0xf bound_ctrl:1
	v_pk_mul_f32 v[34:35], v[34:35], v[38:39]
	v_cvt_pk_bf16_f32 v29, v40, v41
	v_cndmask_b32_e64 v35, v35, -v35, s[38:39]
	v_cndmask_b32_e64 v34, v34, -v34, s[38:39]
	v_pk_fma_f32 v[32:33], v[50:51], v[32:33], v[34:35]
	v_cvt_pk_bf16_f32 v30, v44, v45
	v_pk_mul_f32 v[38:39], v[88:89], v[32:33]
	v_cvt_pk_bf16_f32 v32, v82, v83
	v_cvt_pk_bf16_f32 v33, v36, v37
	v_cvt_pk_bf16_f32 v34, v46, v47
	v_cvt_pk_bf16_f32 v31, v42, v43
	v_cvt_pk_bf16_f32 v35, v38, v39
	ds_write_b128 v95, v[28:31] offset:2048
	ds_write_b128 v95, v[32:35] offset:6144
	v_mov_b64_e32 v[42:43], v[18:19]
	v_mov_b64_e32 v[46:47], v[22:23]
	v_mov_b64_e32 v[82:83], v[26:27]
	v_mov_b64_e32 v[50:51], v[2:3]
	v_mov_b64_e32 v[34:35], v[6:7]
	v_mov_b64_e32 v[30:31], v[14:15]
	v_mov_b64_e32 v[38:39], v[10:11]
	s_andn2_b64 vcc, exec, s[26:27]
	v_mov_b64_e32 v[40:41], v[16:17]
	v_mov_b64_e32 v[44:45], v[20:21]
	v_mov_b64_e32 v[80:81], v[24:25]
	v_mov_b64_e32 v[48:49], v[0:1]
	v_mov_b64_e32 v[32:33], v[4:5]
	v_mov_b64_e32 v[28:29], v[12:13]
	v_mov_b64_e32 v[36:37], v[8:9]
	s_cbranch_vccnz .LBB0_920
	v_add_u32_e32 v36, 8, v94
	s_nop 0
	v_ashrrev_i32_e32 v37, 31, v36
	v_mad_i64_i32 v[28:29], s[26:27], v36, s11, v[84:85]
	v_add_co_u32_e32 v48, vcc, 0x1000, v28
	v_lshlrev_b64 v[36:37], 8, v[36:37]
	s_nop 0
	v_addc_co_u32_e32 v49, vcc, 0, v29, vcc
	v_lshl_add_u64 v[80:81], v[174:175], 0, v[36:37]
	global_load_dwordx4 v[28:31], v[28:29], off offset:3584
	s_nop 0
	global_load_dwordx4 v[32:35], v[48:49], off offset:512
	global_load_dwordx4 v[36:39], v[80:81], off offset:48
	global_load_dwordx4 v[40:43], v[80:81], off offset:32
	global_load_dwordx4 v[44:47], v[80:81], off offset:16
	s_nop 0
	global_load_dwordx4 v[48:51], v[48:49], off offset:1536
	s_nop 0
	global_load_dwordx4 v[80:83], v[80:81], off
